# P2 states: next head's conv weights+bias read from an LDS copy made in the unit set-up (5 global loads per head less)
# speedup vs baseline: 1.0081x; 1.0054x over previous
.LBB0_397:
	v_and_b32_e32 v216, 15, v0
	v_bfe_u32 v217, v0, 4, 2
	v_lshrrev_b32_e32 v218, 6, v0
	v_mul_u32_u24_e32 v212, 0x110, v216
	v_lshl_add_u32 v212, v218, 5, v212
	v_lshl_add_u32 v212, v217, 3, v212
	v_add_u32_e32 v212, 0x13000, v212
	v_lshl_add_u32 v213, v218, 3, v217
	v_mul_u32_u24_e32 v213, 0x110, v213
	v_lshl_add_u32 v213, v216, 4, v213
	v_add_u32_e32 v213, 0x13000, v213
	v_mul_u32_u24_e32 v214, 0x7e0, v218
	v_mul_u32_u24_e32 v219, 0xf8, v217
	v_add_u32_e32 v214, v214, v219
	v_mul_u32_u24_e32 v219, 0xf0, v216
	v_sub_u32_e32 v214, v214, v219
	v_add_u32_e32 v214, 0x1000, v214
	v_mov_b32_e32 v215, 0
	v_and_b32_e32 v240, 31, v0
	v_lshlrev_b32_e32 v240, 3, v240
	v_add_u32_e32 v240, 0x1b800, v240
	s_bfe_u32 s56, s55, 0x60003
	s_lshl_b32 s42, s56, 7
	s_and_b32 s39, s55, 7
	s_ashr_i32 s40, s55, 9
	v_or_b32_e32 v2, s42, v23
	s_lshl_b32 s41, s40, 13
	v_lshl_or_b32 v6, s39, 9, v1
	v_cmp_eq_u32_e64 s[12:13], 0, v2
	s_or_b32 s38, s42, s41
	v_lshlrev_b32_e32 v20, 1, v6
	v_cndmask_b32_e64 v42, v58, 0, s[12:13]
	v_lshl_add_u64 v[2:3], s[2:3], 0, v[20:21]
	v_add_u32_e32 v4, s38, v42
	v_mad_i64_i32 v[4:5], s[58:59], v4, s45, v[2:3]
	v_cndmask_b32_e64 v40, v59, 0, s[12:13]
	global_load_dword v49, v[4:5], off
	v_add_u32_e32 v4, s38, v40
	v_mad_i64_i32 v[4:5], s[58:59], v4, s45, v[2:3]
	v_cndmask_b32_e64 v38, v60, 0, s[12:13]
	global_load_dword v50, v[4:5], off
	v_add_u32_e32 v4, s38, v38
	v_mad_i64_i32 v[4:5], s[58:59], v4, s45, v[2:3]
	global_load_dword v51, v[4:5], off
	v_or_b32_e32 v4, s38, v23
	v_mad_i64_i32 v[4:5], s[58:59], v4, s45, v[2:3]
	global_load_dword v45, v[4:5], off
	v_or_b32_e32 v4, s38, v61
	v_mad_i64_i32 v[4:5], s[58:59], v4, s45, v[2:3]
	global_load_dword v46, v[4:5], off
	v_or_b32_e32 v4, s38, v62
	v_mad_i64_i32 v[4:5], s[58:59], v4, s45, v[2:3]
	global_load_dword v48, v[4:5], off
	v_or_b32_e32 v4, s38, v63
	v_mad_i64_i32 v[4:5], s[58:59], v4, s45, v[2:3]
	global_load_dword v44, v[4:5], off
	v_or_b32_e32 v4, s38, v64
	v_mad_i64_i32 v[4:5], s[58:59], v4, s45, v[2:3]
	global_load_dword v47, v[4:5], off
	v_or_b32_e32 v4, s38, v65
	v_mad_i64_i32 v[4:5], s[58:59], v4, s45, v[2:3]
	global_load_dword v41, v[4:5], off
	v_or_b32_e32 v4, s38, v66
	v_mad_i64_i32 v[4:5], s[58:59], v4, s45, v[2:3]
	v_readlane_b32 s60, v253, 18
	global_load_dword v43, v[4:5], off
	v_or_b32_e32 v4, s38, v67
	v_readlane_b32 s74, v253, 32
	v_readlane_b32 s75, v253, 33
	v_mad_i64_i32 v[2:3], s[58:59], v4, s45, v[2:3]
	v_readlane_b32 s68, v253, 26
	v_readlane_b32 s69, v253, 27
	v_readlane_b32 s70, v253, 28
	v_readlane_b32 s71, v253, 29
	v_readlane_b32 s72, v253, 30
	v_readlane_b32 s73, v253, 31
	s_mov_b32 s26, s84
	s_mov_b64 s[90:91], s[74:75]
	global_load_dword v39, v[2:3], off
	v_lshlrev_b32_e32 v2, 2, v6
	s_mov_b64 s[86:87], s[70:71]
	s_mov_b64 s[88:89], s[72:73]
	global_load_dwordx2 v[12:13], v2, s[86:87]
	global_load_dwordx2 v[16:17], v2, s[18:19]
	global_load_dwordx2 v[10:11], v2, s[20:21]
	global_load_dwordx2 v[18:19], v2, s[22:23]
	global_load_dwordx2 v[14:15], v2, s[88:89]
	v_or_b32_e32 v2, s38, v248
	v_ashrrev_i32_e32 v3, 31, v2
	v_lshlrev_b64 v[4:5], 8, v[2:3]
	v_or_b32_e32 v2, 64, v2
	s_mov_b64 s[84:85], s[68:69]
	s_lshl_b32 s57, s39, 3
	v_ashrrev_i32_e32 v3, 31, v2
	s_mov_b32 s84, s26
	s_add_i32 s26, s57, s26
	v_lshlrev_b64 v[2:3], 8, v[2:3]
	v_readlane_b32 s61, v253, 19
	v_readlane_b32 s62, v253, 20
	v_readlane_b32 s63, v253, 21
	v_readlane_b32 s64, v253, 22
	v_readlane_b32 s65, v253, 23
	v_readlane_b32 s66, v253, 24
	v_readlane_b32 s67, v253, 25
	v_lshl_add_u64 v[4:5], s[24:25], 0, v[4:5]
	s_lshl_b32 s26, s26, 2
	v_lshl_add_u64 v[2:3], s[24:25], 0, v[2:3]
	v_lshl_add_u64 v[4:5], v[4:5], 0, s[26:27]
	v_lshl_add_u64 v[2:3], v[2:3], 0, s[26:27]
	v_readlane_b32 s60, v253, 34
	v_lshl_or_b32 v6, s39, 7, v68
	v_cmp_gt_i32_e32 vcc, s42, v102
	global_load_dword v29, v[4:5], off
	global_load_dword v32, v[2:3], off
	v_mov_b32_e32 v2, s26
	v_readlane_b32 s61, v253, 35
	v_lshlrev_b32_e32 v20, 1, v6
	v_cndmask_b32_e32 v4, 0, v70, vcc
	global_load_dword v33, v2, s[90:91]
	v_add_u32_e32 v4, s38, v4
	v_or_b32_e32 v7, s38, v69
	global_load_dword v34, v2, s[60:61]
	v_lshl_add_u64 v[2:3], s[2:3], 0, v[20:21]
	v_mad_i64_i32 v[4:5], s[58:59], v4, s45, v[2:3]
	global_load_dword v20, v[4:5], off
	v_cndmask_b32_e32 v4, 0, v71, vcc
	v_add_u32_e32 v4, s38, v4
	v_mad_i64_i32 v[4:5], s[58:59], v4, s45, v[2:3]
	global_load_dword v30, v[4:5], off
	v_cndmask_b32_e32 v4, 0, v72, vcc
	v_add_u32_e32 v4, s38, v4
	v_mad_i64_i32 v[4:5], s[58:59], v4, s45, v[2:3]
	global_load_dword v31, v[4:5], off
	v_mad_i64_i32 v[4:5], s[58:59], v7, s45, v[2:3]
	global_load_dword v122, v[4:5], off
	v_or_b32_e32 v4, 1, v7
	v_mad_i64_i32 v[4:5], s[58:59], v4, s45, v[2:3]
	global_load_dword v123, v[4:5], off
	v_or_b32_e32 v4, 2, v7
	v_mad_i64_i32 v[4:5], s[58:59], v4, s45, v[2:3]
	global_load_dword v124, v[4:5], off
	v_or_b32_e32 v4, 3, v7
	v_mad_i64_i32 v[4:5], s[58:59], v4, s45, v[2:3]
	global_load_dword v120, v[4:5], off
	v_or_b32_e32 v4, 4, v7
	v_mad_i64_i32 v[4:5], s[58:59], v4, s45, v[2:3]
	global_load_dword v121, v[4:5], off
	v_or_b32_e32 v4, 5, v7
	v_mad_i64_i32 v[4:5], s[58:59], v4, s45, v[2:3]
	global_load_dword v118, v[4:5], off
	v_or_b32_e32 v4, 6, v7
	v_mad_i64_i32 v[4:5], s[58:59], v4, s45, v[2:3]
	global_load_dword v119, v[4:5], off
	v_or_b32_e32 v4, s38, v103
	v_mad_i64_i32 v[4:5], s[58:59], v4, s45, v[2:3]
	global_load_dword v117, v[4:5], off
	v_or_b32_e32 v4, s38, v74
	v_mad_i64_i32 v[4:5], s[58:59], v4, s45, v[2:3]
	global_load_dword v113, v[4:5], off
	v_or_b32_e32 v4, s38, v75
	v_mad_i64_i32 v[4:5], s[58:59], v4, s45, v[2:3]
	global_load_dword v116, v[4:5], off
	v_or_b32_e32 v4, s38, v76
	v_mad_i64_i32 v[4:5], s[58:59], v4, s45, v[2:3]
	global_load_dword v114, v[4:5], off
	v_or_b32_e32 v4, s38, v73
	v_mad_i64_i32 v[4:5], s[58:59], v4, s45, v[2:3]
	global_load_dword v57, v[4:5], off
	v_or_b32_e32 v4, s38, v77
	v_mad_i64_i32 v[4:5], s[58:59], v4, s45, v[2:3]
	global_load_dword v112, v[4:5], off
	v_or_b32_e32 v4, s38, v78
	v_mad_i64_i32 v[4:5], s[58:59], v4, s45, v[2:3]
	global_load_dword v115, v[4:5], off
	v_or_b32_e32 v4, s38, v79
	v_mad_i64_i32 v[4:5], s[58:59], v4, s45, v[2:3]
	global_load_dword v55, v[4:5], off
	v_or_b32_e32 v4, s38, v80
	v_mad_i64_i32 v[4:5], s[58:59], v4, s45, v[2:3]
	global_load_dword v56, v[4:5], off
	v_or_b32_e32 v4, s38, v81
	v_mad_i64_i32 v[4:5], s[58:59], v4, s45, v[2:3]
	global_load_dword v53, v[4:5], off
	v_or_b32_e32 v4, s38, v82
	v_mad_i64_i32 v[4:5], s[58:59], v4, s45, v[2:3]
	global_load_dword v54, v[4:5], off
	v_or_b32_e32 v4, s38, v83
	v_mad_i64_i32 v[2:3], s[38:39], v4, s45, v[2:3]
	v_lshlrev_b32_e32 v6, 2, v6
	global_load_dword v52, v[2:3], off
	global_load_dwordx2 v[4:5], v6, s[86:87]
	global_load_dwordx2 v[8:9], v6, s[18:19]
	s_nop 0
	global_load_dwordx2 v[2:3], v6, s[20:21]
	global_load_dwordx2 v[36:37], v6, s[22:23]
	s_nop 0
	global_load_dwordx2 v[6:7], v6, s[88:89]
	s_waitcnt vmcnt(28)
	v_add_f32_e32 v29, v29, v33
	v_cmp_nlt_f32_e32 vcc, s46, v29
	v_readlane_b32 s62, v253, 36
	v_readlane_b32 s63, v253, 37
	v_readlane_b32 s64, v253, 38
	v_readlane_b32 s65, v253, 39
	v_readlane_b32 s66, v253, 40
	v_readlane_b32 s67, v253, 41
	v_readlane_b32 s68, v253, 42
	v_readlane_b32 s69, v253, 43
	v_readlane_b32 s70, v253, 44
	v_readlane_b32 s71, v253, 45
	v_readlane_b32 s72, v253, 46
	v_readlane_b32 s73, v253, 47
	v_readlane_b32 s74, v253, 48
	v_readlane_b32 s75, v253, 49
	s_barrier
	s_and_saveexec_b64 s[38:39], vcc
	s_cbranch_execz .LBB0_399
	v_mul_f32_e32 v29, 0x3fb8aa3b, v29
	v_exp_f32_e32 v35, v29
	s_nop 0
	v_add_f32_e32 v29, 1.0, v35
	v_frexp_mant_f32_e32 v128, v29
	v_cvt_f64_f32_e32 v[126:127], v29
	v_add_f32_e32 v125, -1.0, v29
	v_frexp_exp_i32_f64_e32 v126, v[126:127]
	v_cmp_gt_f32_e32 vcc, s47, v128
	v_sub_f32_e32 v129, v125, v29
	v_sub_f32_e32 v125, v35, v125
	v_subbrev_co_u32_e32 v134, vcc, 0, v126, vcc
	v_add_f32_e32 v129, 1.0, v129
	v_sub_u32_e32 v126, 0, v134
	v_add_f32_e32 v125, v125, v129
	v_ldexp_f32 v29, v29, v126
	v_ldexp_f32 v125, v125, v126
	v_add_f32_e32 v126, -1.0, v29
	v_add_f32_e32 v127, 1.0, v126
	v_sub_f32_e32 v127, v29, v127
	v_add_f32_e32 v128, v125, v127
	v_add_f32_e32 v127, 1.0, v29
	v_add_f32_e32 v129, -1.0, v127
	v_sub_f32_e32 v29, v29, v129
	v_add_f32_e32 v29, v125, v29
	v_add_f32_e32 v125, v127, v29
	v_rcp_f32_e32 v135, v125
	v_sub_f32_e32 v127, v125, v127
	v_sub_f32_e32 v29, v29, v127
	v_add_f32_e32 v127, v126, v128
	v_sub_f32_e32 v126, v127, v126
	v_mul_f32_e32 v137, v127, v135
	v_sub_f32_e32 v136, v128, v126
	v_mul_f32_e32 v128, v125, v137
	v_fma_f32 v130, v137, v125, -v128
	v_fmac_f32_e32 v130, v137, v29
	v_add_f32_e32 v126, v128, v130
	v_sub_f32_e32 v129, v127, v126
	v_pk_add_f32 v[132:133], v[126:127], v[128:129] neg_lo:[0,1] neg_hi:[0,1]
	v_mov_b32_e32 v131, v126
	v_pk_add_f32 v[126:127], v[132:133], v[130:131] neg_lo:[0,1] neg_hi:[0,1]
	v_cmp_neq_f32_e32 vcc, s50, v35
	v_add_f32_e32 v127, v136, v127
	v_add_f32_e32 v126, v126, v127
	v_add_f32_e32 v127, v129, v126
	v_mul_f32_e32 v136, v135, v127
	v_mul_f32_e32 v128, v125, v136
	v_fma_f32 v130, v136, v125, -v128
	v_fmac_f32_e32 v130, v136, v29
	v_sub_f32_e32 v29, v129, v127
	v_add_f32_e32 v29, v126, v29
	v_add_f32_e32 v126, v128, v130
	v_sub_f32_e32 v129, v127, v126
	v_pk_add_f32 v[132:133], v[126:127], v[128:129] neg_lo:[0,1] neg_hi:[0,1]
	v_mov_b32_e32 v131, v126
	v_pk_add_f32 v[126:127], v[132:133], v[130:131] neg_lo:[0,1] neg_hi:[0,1]
	v_add_f32_e32 v125, v137, v136
	v_add_f32_e32 v29, v29, v127
	v_add_f32_e32 v29, v126, v29
	v_add_f32_e32 v29, v129, v29
	v_sub_f32_e32 v126, v125, v137
	v_mul_f32_e32 v29, v135, v29
	v_sub_f32_e32 v126, v136, v126
	v_add_f32_e32 v127, v126, v29
	v_add_f32_e32 v128, v125, v127
	v_cvt_f32_i32_e32 v126, v134
	v_mul_f32_e32 v130, v128, v128
	v_fmamk_f32 v29, v130, 0x3e9b6dac, v105
	v_sub_f32_e32 v125, v128, v125
	v_fmaak_f32 v29, v130, v29, 0x3f2aaada
	v_sub_f32_e32 v125, v127, v125
	v_mul_f32_e32 v127, v128, v130
	v_pk_mul_f32 v[130:131], v[126:127], v[28:29]
	v_ldexp_f32 v129, v128, 1
	v_fma_f32 v128, v126, s49, -v130
	v_fmac_f32_e32 v128, 0xb102e308, v126
	v_pk_add_f32 v[126:127], v[130:131], v[128:129]
	v_ldexp_f32 v125, v125, 1
	v_sub_f32_e32 v29, v127, v129
	v_sub_f32_e32 v29, v131, v29
	v_add_f32_e32 v133, v125, v29
	v_mov_b32_e32 v132, v130
	v_pk_add_f32 v[130:131], v[126:127], v[130:131] neg_lo:[0,1] neg_hi:[0,1]
	v_pk_add_f32 v[134:135], v[126:127], v[132:133]
	v_mov_b32_e32 v129, v126
	v_mov_b32_e32 v131, v135
	v_pk_add_f32 v[136:137], v[128:129], v[130:131] neg_lo:[0,1] neg_hi:[0,1]
	v_pk_add_f32 v[128:129], v[128:129], v[130:131]
	v_mov_b32_e32 v132, v133
	v_pk_add_f32 v[130:131], v[128:129], v[126:127] op_sel:[1,0] op_sel_hi:[0,1] neg_lo:[0,1] neg_hi:[0,1]
	v_pk_add_f32 v[138:139], v[134:135], v[130:131] op_sel_hi:[1,0] neg_lo:[0,1] neg_hi:[0,1]
	v_mov_b32_e32 v134, v135
	v_mov_b32_e32 v135, v129
	v_pk_mov_b32 v[130:131], v[126:127], v[130:131] op_sel:[1,0]
	v_mov_b32_e32 v133, v126
	v_pk_add_f32 v[130:131], v[134:135], v[130:131] neg_lo:[0,1] neg_hi:[0,1]
	v_mov_b32_e32 v138, v136
	v_pk_add_f32 v[126:127], v[132:133], v[130:131] neg_lo:[0,1] neg_hi:[0,1]
	v_mov_b32_e32 v137, v129
	v_pk_add_f32 v[130:131], v[138:139], v[126:127]
	s_nop 0
	v_pk_add_f32 v[132:133], v[130:131], v[130:131] op_sel:[0,1] op_sel_hi:[1,0]
	s_nop 0
	v_pk_add_f32 v[128:129], v[128:129], v[132:133] op_sel:[1,0] op_sel_hi:[0,1]
	v_mov_b32_e32 v131, v128
	v_pk_add_f32 v[134:135], v[130:131], v[136:137] neg_lo:[0,1] neg_hi:[0,1]
	v_mov_b32_e32 v127, v132
	v_sub_f32_e32 v29, v130, v134
	v_pk_add_f32 v[126:127], v[126:127], v[134:135] neg_lo:[0,1] neg_hi:[0,1]
	v_sub_f32_e32 v29, v136, v29
	v_add_f32_e32 v29, v126, v29
	v_add_f32_e32 v29, v29, v127
	v_add_f32_e32 v29, v128, v29
	v_cndmask_b32_e32 v29, v109, v29, vcc
	v_cmp_ngt_f32_e32 vcc, -1.0, v35
	s_nop 1
	v_cndmask_b32_e32 v29, v110, v29, vcc
	v_cmp_neq_f32_e32 vcc, -1.0, v35
	s_nop 1
	v_cndmask_b32_e32 v29, v111, v29, vcc
	v_cmp_lt_f32_e64 vcc, |v35|, s51
	s_nop 1
	v_cndmask_b32_e32 v29, v29, v35, vcc

.LBB0_401:
	s_or_b64 exec, exec, s[38:39]
	v_mul_f32_e64 v32, v29, -v35
	ds_bpermute_b32 v33, v96, v32
	v_or_b32_e32 v125, s42, v69
	v_cmp_eq_u32_e32 vcc, 0, v125
	s_and_b32 s43, s54, 7
	s_lshl_b32 s38, s43, 9
	s_waitcnt lgkmcnt(0)
	v_fma_f32 v33, v29, -v35, v33
	v_cndmask_b32_e64 v32, v33, v32, s[0:1]
	ds_bpermute_b32 v33, v97, v32
	s_waitcnt vmcnt(26)
	v_cndmask_b32_e64 v20, v20, 0, vcc
	s_waitcnt vmcnt(25)
	v_cndmask_b32_e64 v126, v30, 0, vcc
	s_waitcnt vmcnt(24)
	v_cndmask_b32_e64 v134, v31, 0, vcc
	v_lshlrev_b32_e32 v30, 16, v20
	s_waitcnt lgkmcnt(0)
	v_add_f32_e32 v33, v32, v33
	v_cndmask_b32_e64 v32, v33, v32, s[14:15]
	ds_bpermute_b32 v33, v98, v32
	v_and_b32_e32 v31, 0xffff0000, v20
	s_waitcnt vmcnt(0)
	v_fma_f32 v128, v4, v30, v6
	v_or_b32_e32 v35, s38, v1
	v_readlane_b32 s60, v253, 18
	s_waitcnt lgkmcnt(0)
	v_add_f32_e32 v33, v32, v33
	v_cndmask_b32_e64 v32, v33, v32, s[4:5]
	ds_bpermute_b32 v33, v99, v32
	v_readlane_b32 s70, v253, 28
	v_readlane_b32 s71, v253, 29
	v_fma_f32 v135, v5, v31, v7
	v_lshlrev_b32_e32 v125, 16, v126
	s_waitcnt lgkmcnt(0)
	v_add_f32_e32 v20, v32, v33
	v_cndmask_b32_e64 v32, v20, v32, s[6:7]
	ds_bpermute_b32 v33, v100, v32
	v_lshlrev_b32_e32 v20, 2, v35
	v_lshlrev_b32_e32 v130, 16, v122
	v_lshlrev_b32_e32 v131, 16, v134
	v_fmac_f32_e32 v128, v8, v125
	s_waitcnt lgkmcnt(0)
	v_add_f32_e32 v30, v32, v33
	v_cndmask_b32_e64 v127, v30, v32, s[8:9]
	ds_bpermute_b32 v129, v101, v127
	v_lshl_add_u64 v[30:31], s[30:31], 0, v[20:21]
	v_lshl_add_u64 v[32:33], s[70:71], 0, v[20:21]
	v_lshrrev_b32_e32 v220, 5, v0
	v_and_b32_e32 v221, 7, v220
	v_lshrrev_b32_e32 v220, 3, v220
	v_lshlrev_b32_e32 v222, 8, v221
	v_mul_u32_u24_e32 v224, 0x12000, v220
	v_add_u32_e32 v224, v224, v222
	v_mov_b32_e32 v225, 0
	v_mov_b32_e32 v229, 0
	v_lshl_add_u64 v[226:227], v[32:33], 0, v[224:225]
	global_load_dwordx2 v[234:235], v[226:227], off
	v_sub_u32_e32 v223, 1, v220
	v_mul_u32_u24_e32 v228, 0xc000, v223
	v_lshl_add_u64 v[226:227], v[226:227], 0, v[228:229]
	global_load_dwordx2 v[236:237], v[226:227], off
	v_cmp_eq_u32_e64 s[76:77], 1, v220
	v_mul_u32_u24_e32 v228, 0x6000, v223
	v_add_u32_e32 v228, v228, v222
	v_lshlrev_b32_e32 v231, 8, v220
	v_sub_u32_e32 v228, v228, v231
	v_ashrrev_i32_e32 v229, 31, v228
	v_cndmask_b32_e64 v226, v32, v30, s[76:77]
	v_cndmask_b32_e64 v227, v33, v31, s[76:77]
	v_lshl_add_u64 v[226:227], v[226:227], 0, v[228:229]
	global_load_dwordx2 v[238:239], v[226:227], off
	v_and_b32_e32 v230, 31, v0
	v_lshlrev_b32_e32 v230, 3, v230
	v_mul_u32_u24_e32 v231, 0x500, v221
	v_add_u32_e32 v230, v230, v231
	v_add_u32_e32 v230, 0x1b800, v230
	v_mul_u32_u24_e32 v231, 0x300, v220
	v_add_u32_e32 v232, v230, v231
	v_lshl_add_u32 v233, v220, 8, v230
	v_lshlrev_b32_e32 v20, 1, v35
	v_and_b32_e32 v122, 0xffff0000, v122
	s_waitcnt lgkmcnt(0)
	v_add_f32_e32 v35, v127, v129
	v_cndmask_b32_e64 v35, v35, v127, s[10:11]
	v_add_f32_e32 v34, v35, v34
	ds_write2st64_b32 v84, v29, v34 offset0:1 offset1:17
	v_mov_b32_e32 v34, v36
	v_mov_b32_e32 v35, v2
	v_pk_mul_f32 v[132:133], v[34:35], v[130:131]
	v_and_b32_e32 v127, 0xffff0000, v126
	v_add_f32_e32 v2, v133, v128
	v_add_f32_e32 v29, v132, v2
	v_mul_f32_e32 v2, 0xbfb8aa3b, v29
	v_exp_f32_e32 v2, v2
	v_lshlrev_b32_e32 v129, 16, v123
	v_lshlrev_b32_e32 v128, 16, v124
	v_and_b32_e32 v133, 0xffff0000, v123
	v_add_f32_e32 v2, 1.0, v2
	v_and_b32_e32 v132, 0xffff0000, v124
	v_rcp_f32_e32 v124, v2
	v_and_b32_e32 v123, 0xffff0000, v134
	v_mov_b32_e32 v2, v37
	v_fmac_f32_e32 v135, v9, v127
	v_pk_mul_f32 v[36:37], v[2:3], v[122:123]
	v_mul_f32_e32 v29, v29, v124
	v_add_f32_e32 v37, v37, v135
	v_add_f32_e32 v126, v36, v37
	v_mul_f32_e32 v36, 0xbfb8aa3b, v126
	v_exp_f32_e32 v134, v36
	v_mov_b32_e32 v37, v4
	v_mov_b32_e32 v36, v8
	v_mov_b32_e32 v124, v131
	v_add_f32_e32 v4, 1.0, v134
	v_rcp_f32_e32 v4, v4
	v_pk_mul_f32 v[124:125], v[36:37], v[124:125]
	v_pk_mul_f32 v[134:135], v[36:37], v[130:131]
	v_add_f32_e32 v125, v125, v6
	v_mul_f32_e32 v138, v126, v4
	v_mov_b32_e32 v4, v9
	v_mov_b32_e32 v126, v123
	v_pk_mul_f32 v[8:9], v[4:5], v[126:127]
	v_pk_mov_b32 v[126:127], v[128:129], v[130:131] op_sel:[1,0]
	v_add_f32_e32 v124, v124, v125
	v_pk_mul_f32 v[130:131], v[34:35], v[126:127]
	v_add_f32_e32 v135, v135, v6
	v_add_f32_e32 v124, v131, v124
	v_add_f32_e32 v139, v130, v124
	v_mul_f32_e32 v124, 0xbfb8aa3b, v139
	v_exp_f32_e32 v136, v124
	v_add_f32_e32 v134, v134, v135
	v_lshlrev_b32_e32 v131, 16, v120
	v_and_b32_e32 v135, 0xffff0000, v120
	v_add_f32_e32 v136, 1.0, v136
	v_rcp_f32_e32 v140, v136
	v_pk_mul_f32 v[136:137], v[34:35], v[128:129]
	v_lshlrev_b32_e32 v130, 16, v121
	v_add_f32_e32 v134, v137, v134
	v_add_f32_e32 v136, v136, v134
	v_mul_f32_e32 v134, 0xbfb8aa3b, v136
	v_exp_f32_e32 v137, v134
	v_and_b32_e32 v134, 0xffff0000, v121
	v_add_f32_e32 v9, v9, v7
	v_pk_mul_f32 v[124:125], v[4:5], v[122:123]
	v_add_f32_e32 v120, 1.0, v137
	v_rcp_f32_e32 v137, v120
	v_pk_mov_b32 v[120:121], v[132:133], v[122:123] op_sel:[1,0]
	v_add_f32_e32 v8, v8, v9
	v_pk_mul_f32 v[122:123], v[2:3], v[120:121]
	v_mul_f32_e32 v139, v139, v140
	v_add_f32_e32 v8, v123, v8
	v_add_f32_e32 v140, v122, v8
	v_mul_f32_e32 v8, 0xbfb8aa3b, v140
	v_add_f32_e32 v123, v125, v7
	v_exp_f32_e32 v122, v8
	v_pk_mul_f32 v[8:9], v[2:3], v[132:133]
	v_add_f32_e32 v123, v124, v123
	v_add_f32_e32 v9, v9, v123
	v_add_f32_e32 v124, v8, v9
	v_mul_f32_e32 v8, 0xbfb8aa3b, v124
	v_exp_f32_e32 v8, v8
	v_add_f32_e32 v9, 1.0, v122
	v_mul_f32_e32 v136, v136, v137
	v_rcp_f32_e32 v125, v9
	v_add_f32_e32 v8, 1.0, v8
	v_rcp_f32_e32 v137, v8
	v_pk_mul_f32 v[8:9], v[36:37], v[126:127]
	v_mul_f32_e32 v140, v140, v125
	v_add_f32_e32 v9, v9, v6
	v_mul_f32_e32 v137, v124, v137
	v_pk_mov_b32 v[124:125], v[130:131], v[128:129] op_sel:[1,0]
	v_add_f32_e32 v8, v8, v9
	v_pk_mul_f32 v[126:127], v[34:35], v[124:125]
	v_pk_mul_f32 v[122:123], v[36:37], v[128:129]
	v_add_f32_e32 v8, v127, v8
	v_add_f32_e32 v141, v126, v8
	v_mul_f32_e32 v8, 0xbfb8aa3b, v141
	v_exp_f32_e32 v128, v8
	v_add_f32_e32 v123, v123, v6
	v_add_f32_e32 v122, v122, v123
	v_pk_mul_f32 v[120:121], v[4:5], v[120:121]
	v_add_f32_e32 v128, 1.0, v128
	v_rcp_f32_e32 v142, v128
	v_pk_mul_f32 v[128:129], v[34:35], v[130:131]
	v_lshlrev_b32_e32 v127, 16, v118
	v_add_f32_e32 v122, v129, v122
	v_add_f32_e32 v143, v128, v122
	v_mul_f32_e32 v122, 0xbfb8aa3b, v143
	v_exp_f32_e32 v128, v122
	v_and_b32_e32 v123, 0xffff0000, v118
	v_lshlrev_b32_e32 v126, 16, v119
	v_and_b32_e32 v122, 0xffff0000, v119
	v_add_f32_e32 v118, 1.0, v128
	v_mul_f32_e32 v141, v141, v142
	v_rcp_f32_e32 v142, v118
	v_pk_mov_b32 v[118:119], v[134:135], v[132:133] op_sel:[1,0]
	v_add_f32_e32 v121, v121, v7
	v_pk_mul_f32 v[128:129], v[2:3], v[118:119]
	v_add_f32_e32 v120, v120, v121
	v_add_f32_e32 v120, v129, v120
	v_pk_mul_f32 v[8:9], v[4:5], v[132:133]
	v_add_f32_e32 v132, v128, v120
	v_mul_f32_e32 v120, 0xbfb8aa3b, v132
	v_exp_f32_e32 v128, v120
	v_add_f32_e32 v9, v9, v7
	v_add_f32_e32 v8, v8, v9
	v_mul_f32_e32 v142, v143, v142
	v_add_f32_e32 v128, 1.0, v128
	v_rcp_f32_e32 v133, v128
	v_pk_mul_f32 v[128:129], v[2:3], v[134:135]
	v_pk_mul_f32 v[120:121], v[36:37], v[124:125]
	v_add_f32_e32 v8, v129, v8
	v_add_f32_e32 v143, v128, v8
	v_mul_f32_e32 v8, 0xbfb8aa3b, v143
	v_exp_f32_e32 v144, v8
	v_pk_mov_b32 v[8:9], v[126:127], v[130:131] op_sel:[1,0]
	v_add_f32_e32 v121, v121, v6
	v_pk_mul_f32 v[128:129], v[34:35], v[8:9]
	v_add_f32_e32 v120, v120, v121
	v_add_f32_e32 v120, v129, v120
	v_add_f32_e32 v128, v128, v120
	v_mul_f32_e32 v120, 0xbfb8aa3b, v128
	v_exp_f32_e32 v120, v120
	v_pk_mul_f32 v[118:119], v[4:5], v[118:119]
	v_pk_mul_f32 v[124:125], v[36:37], v[130:131]
	v_pk_mov_b32 v[130:131], v[122:123], v[134:135] op_sel:[1,0]
	v_add_f32_e32 v120, 1.0, v120
	v_rcp_f32_e32 v129, v120
	v_add_f32_e32 v119, v119, v7
	v_add_f32_e32 v121, 1.0, v144
	v_mul_f32_e32 v144, v132, v133
	v_pk_mul_f32 v[132:133], v[2:3], v[130:131]
	v_add_f32_e32 v118, v118, v119
	v_add_f32_e32 v118, v133, v118
	v_mul_f32_e32 v145, v128, v129
	v_pk_mul_f32 v[128:129], v[34:35], v[126:127]
	v_add_f32_e32 v127, v132, v118
	v_rcp_f32_e32 v121, v121
	v_mul_f32_e32 v118, 0xbfb8aa3b, v127
	v_exp_f32_e32 v118, v118
	v_add_f32_e32 v125, v125, v6
	v_mul_f32_e32 v143, v143, v121
	v_pk_mul_f32 v[120:121], v[4:5], v[134:135]
	v_add_f32_e32 v119, v124, v125
	v_add_f32_e32 v119, v129, v119
	v_add_f32_e32 v118, 1.0, v118
	v_add_f32_e32 v121, v121, v7
	v_add_f32_e32 v124, v128, v119
	v_rcp_f32_e32 v125, v118
	v_pk_mul_f32 v[118:119], v[2:3], v[122:123]
	v_add_f32_e32 v120, v120, v121
	v_add_f32_e32 v119, v119, v120
	v_add_f32_e32 v123, v118, v119
	v_mul_f32_e32 v118, 0xbfb8aa3b, v124
	v_exp_f32_e32 v118, v118
	v_mul_f32_e32 v119, 0xbfb8aa3b, v123
	v_exp_f32_e32 v119, v119
	v_pk_mul_f32 v[8:9], v[36:37], v[8:9]
	v_lshlrev_b32_e32 v120, 16, v117
	v_mov_b32_e32 v121, v126
	v_add_f32_e32 v9, v9, v6
	v_add_f32_e32 v118, 1.0, v118
	v_pk_mul_f32 v[120:121], v[34:35], v[120:121]
	v_add_f32_e32 v8, v8, v9
	v_mul_f32_e32 v125, v127, v125
	v_rcp_f32_e32 v127, v118
	v_add_f32_e32 v128, 1.0, v119
	v_pk_mul_f32 v[118:119], v[4:5], v[130:131]
	v_add_f32_e32 v8, v121, v8
	v_add_f32_e32 v120, v120, v8
	v_and_b32_e32 v8, 0xffff0000, v117
	v_mov_b32_e32 v9, v122
	v_add_f32_e32 v117, v119, v7
	v_pk_mul_f32 v[8:9], v[2:3], v[8:9]
	v_add_f32_e32 v117, v118, v117
	v_add_f32_e32 v9, v9, v117
	v_add_f32_e32 v8, v8, v9
	v_mul_f32_e32 v9, 0xbfb8aa3b, v120
	v_mul_f32_e32 v117, 0xbfb8aa3b, v8
	v_exp_f32_e32 v9, v9
	v_exp_f32_e32 v117, v117
	v_rcp_f32_e32 v118, v128
	v_mul_f32_e32 v121, v124, v127
	v_add_f32_e32 v9, 1.0, v9
	v_add_f32_e32 v117, 1.0, v117
	v_rcp_f32_e32 v9, v9
	v_rcp_f32_e32 v117, v117
	v_mul_f32_e32 v126, v123, v118
	v_cvt_pk_bf16_f32 v118, v29, v139
	v_mul_f32_e32 v9, v120, v9
	v_mul_f32_e32 v8, v8, v117
	v_cvt_pk_bf16_f32 v119, v136, v141
	v_cvt_pk_bf16_f32 v120, v142, v145
	v_cvt_pk_bf16_f32 v121, v121, v9
	v_cvt_pk_bf16_f32 v122, v138, v140
	v_cvt_pk_bf16_f32 v123, v137, v144
	v_cvt_pk_bf16_f32 v124, v143, v125
	v_cvt_pk_bf16_f32 v125, v126, v8
	v_lshlrev_b32_e32 v8, 16, v116
	v_lshlrev_b32_e32 v9, 16, v113
	ds_write_b128 v85, v[118:121] offset:8192
	ds_write_b128 v85, v[122:125] offset:8464
	v_pk_mul_f32 v[118:119], v[36:37], v[8:9]
	v_lshlrev_b32_e32 v123, 16, v114
	v_lshlrev_b32_e32 v122, 16, v57
	v_add_f32_e32 v9, v119, v6
	v_pk_mul_f32 v[126:127], v[34:35], v[122:123]
	v_add_f32_e32 v9, v118, v9
	v_add_f32_e32 v9, v127, v9
	v_and_b32_e32 v117, 0xffff0000, v113
	v_and_b32_e32 v116, 0xffff0000, v116
	v_add_f32_e32 v9, v126, v9
	v_pk_mul_f32 v[120:121], v[4:5], v[116:117]
	v_mul_f32_e32 v29, 0xbfb8aa3b, v9
	v_and_b32_e32 v125, 0xffff0000, v114
	v_exp_f32_e32 v29, v29
	v_and_b32_e32 v124, 0xffff0000, v57
	v_add_f32_e32 v57, v121, v7
	v_pk_mul_f32 v[126:127], v[2:3], v[124:125]
	v_add_f32_e32 v57, v120, v57
	v_add_f32_e32 v57, v127, v57
	v_add_f32_e32 v57, v126, v57
	v_add_f32_e32 v29, 1.0, v29
	v_mul_f32_e32 v113, 0xbfb8aa3b, v57
	v_rcp_f32_e32 v29, v29
	v_exp_f32_e32 v114, v113
	v_lshlrev_b32_e32 v119, 16, v112
	v_lshlrev_b32_e32 v118, 16, v115
	v_mul_f32_e32 v29, v9, v29
	v_add_f32_e32 v9, 1.0, v114
	v_rcp_f32_e32 v120, v9
	v_pk_mov_b32 v[8:9], v[122:123], v[8:9] op_sel:[1,0]
	v_and_b32_e32 v113, 0xffff0000, v112
	v_pk_mul_f32 v[8:9], v[36:37], v[8:9]
	v_mul_f32_e32 v128, v57, v120
	v_pk_mov_b32 v[120:121], v[118:119], v[122:123] op_sel:[1,0]
	v_add_f32_e32 v9, v9, v6
	v_and_b32_e32 v112, 0xffff0000, v115
	v_pk_mul_f32 v[114:115], v[36:37], v[122:123]
	v_pk_mul_f32 v[122:123], v[34:35], v[120:121]
	v_add_f32_e32 v8, v8, v9
	v_add_f32_e32 v8, v123, v8
	v_add_f32_e32 v129, v122, v8
	v_mul_f32_e32 v8, 0xbfb8aa3b, v129
	v_exp_f32_e32 v57, v8
	v_pk_mul_f32 v[126:127], v[34:35], v[118:119]
	v_pk_mov_b32 v[116:117], v[124:125], v[116:117] op_sel:[1,0]
	v_lshlrev_b32_e32 v123, 16, v55
	v_add_f32_e32 v57, 1.0, v57
	v_rcp_f32_e32 v130, v57
	v_add_f32_e32 v57, v115, v6
	v_add_f32_e32 v57, v114, v57
	v_add_f32_e32 v57, v127, v57
	v_add_f32_e32 v126, v126, v57
	v_mul_f32_e32 v57, 0xbfb8aa3b, v126
	v_exp_f32_e32 v114, v57
	v_pk_mul_f32 v[116:117], v[4:5], v[116:117]
	v_and_b32_e32 v57, 0xffff0000, v55
	v_add_f32_e32 v117, v117, v7
	v_add_f32_e32 v55, 1.0, v114
	v_pk_mov_b32 v[114:115], v[112:113], v[124:125] op_sel:[1,0]
	v_pk_mul_f32 v[8:9], v[4:5], v[124:125]
	v_pk_mul_f32 v[124:125], v[2:3], v[114:115]
	v_add_f32_e32 v116, v116, v117
	v_add_f32_e32 v116, v125, v116
	v_add_f32_e32 v124, v124, v116
	v_mul_f32_e32 v116, 0xbfb8aa3b, v124
	v_add_f32_e32 v9, v9, v7
	v_exp_f32_e32 v125, v116
	v_pk_mul_f32 v[116:117], v[2:3], v[112:113]
	v_add_f32_e32 v8, v8, v9
	v_add_f32_e32 v8, v117, v8
	v_mul_f32_e32 v127, v129, v130
	v_add_f32_e32 v129, v116, v8
	v_mul_f32_e32 v8, 0xbfb8aa3b, v129
	v_exp_f32_e32 v8, v8
	v_rcp_f32_e32 v55, v55
	v_add_f32_e32 v9, 1.0, v125
	v_lshlrev_b32_e32 v122, 16, v56
	v_add_f32_e32 v8, 1.0, v8
	v_mul_f32_e32 v126, v126, v55
	v_rcp_f32_e32 v55, v9
	v_rcp_f32_e32 v125, v8
	v_pk_mul_f32 v[8:9], v[36:37], v[120:121]
	v_pk_mul_f32 v[116:117], v[36:37], v[118:119]
	v_pk_mov_b32 v[118:119], v[122:123], v[118:119] op_sel:[1,0]
	v_add_f32_e32 v9, v9, v6
	v_pk_mul_f32 v[120:121], v[34:35], v[118:119]
	v_add_f32_e32 v8, v8, v9
	v_add_f32_e32 v8, v121, v8
	v_add_f32_e32 v131, v120, v8
	v_mul_f32_e32 v8, 0xbfb8aa3b, v131
	v_mul_f32_e32 v130, v124, v55
	v_exp_f32_e32 v55, v8
	v_mul_f32_e32 v129, v129, v125
	v_pk_mul_f32 v[124:125], v[34:35], v[122:123]
	v_and_b32_e32 v56, 0xffff0000, v56
	v_add_f32_e32 v55, 1.0, v55
	v_rcp_f32_e32 v132, v55
	v_add_f32_e32 v55, v117, v6
	v_add_f32_e32 v55, v116, v55
	v_add_f32_e32 v55, v125, v55
	v_add_f32_e32 v124, v124, v55
	v_mul_f32_e32 v55, 0xbfb8aa3b, v124
	v_exp_f32_e32 v116, v55
	v_pk_mul_f32 v[114:115], v[4:5], v[114:115]
	v_pk_mul_f32 v[8:9], v[4:5], v[112:113]
	v_pk_mov_b32 v[112:113], v[56:57], v[112:113] op_sel:[1,0]
	v_add_f32_e32 v116, 1.0, v116
	v_add_f32_e32 v115, v115, v7
	v_rcp_f32_e32 v125, v116
	v_pk_mul_f32 v[116:117], v[2:3], v[112:113]
	v_add_f32_e32 v114, v114, v115
	v_add_f32_e32 v114, v117, v114
	v_lshlrev_b32_e32 v121, 16, v53
	v_and_b32_e32 v55, 0xffff0000, v53
	v_mul_f32_e32 v53, v131, v132
	v_add_f32_e32 v131, v116, v114
	v_mul_f32_e32 v114, 0xbfb8aa3b, v131
	v_exp_f32_e32 v132, v114
	v_pk_mul_f32 v[114:115], v[36:37], v[118:119]
	v_add_f32_e32 v9, v9, v7
	v_mul_f32_e32 v124, v124, v125
	v_add_f32_e32 v118, 1.0, v132
	v_rcp_f32_e32 v125, v118
	v_pk_mul_f32 v[118:119], v[2:3], v[56:57]
	v_add_f32_e32 v8, v8, v9
	v_add_f32_e32 v8, v119, v8
	v_add_f32_e32 v132, v118, v8
	v_lshlrev_b32_e32 v120, 16, v54
	v_mul_f32_e32 v8, 0xbfb8aa3b, v132
	v_exp_f32_e32 v133, v8
	v_pk_mov_b32 v[8:9], v[120:121], v[122:123] op_sel:[1,0]
	v_add_f32_e32 v115, v115, v6
	v_pk_mul_f32 v[118:119], v[34:35], v[8:9]
	v_add_f32_e32 v114, v114, v115
	v_add_f32_e32 v114, v119, v114
	v_add_f32_e32 v118, v118, v114
	v_mul_f32_e32 v114, 0xbfb8aa3b, v118
	v_exp_f32_e32 v114, v114
	v_add_f32_e32 v115, 1.0, v133
	v_rcp_f32_e32 v115, v115
	v_and_b32_e32 v54, 0xffff0000, v54
	v_add_f32_e32 v114, 1.0, v114
	v_rcp_f32_e32 v119, v114
	v_pk_mul_f32 v[112:113], v[4:5], v[112:113]
	v_mul_f32_e32 v125, v131, v125
	v_mul_f32_e32 v131, v132, v115
	v_pk_mul_f32 v[114:115], v[4:5], v[56:57]
	v_pk_mov_b32 v[56:57], v[54:55], v[56:57] op_sel:[1,0]
	v_add_f32_e32 v113, v113, v7
	v_pk_mul_f32 v[116:117], v[36:37], v[122:123]
	v_pk_mul_f32 v[122:123], v[2:3], v[56:57]
	v_add_f32_e32 v112, v112, v113
	v_add_f32_e32 v112, v123, v112
	v_mul_f32_e32 v132, v118, v119
	v_pk_mul_f32 v[118:119], v[34:35], v[120:121]
	v_add_f32_e32 v121, v122, v112
	v_mul_f32_e32 v112, 0xbfb8aa3b, v121
	v_exp_f32_e32 v112, v112
	v_add_f32_e32 v117, v117, v6
	v_add_f32_e32 v113, v116, v117
	v_add_f32_e32 v113, v119, v113
	v_add_f32_e32 v112, 1.0, v112
	v_pk_mul_f32 v[8:9], v[36:37], v[8:9]
	v_add_f32_e32 v116, v118, v113
	v_rcp_f32_e32 v117, v112
	v_pk_mul_f32 v[112:113], v[2:3], v[54:55]
	v_add_f32_e32 v55, v115, v7
	v_pk_mul_f32 v[4:5], v[4:5], v[56:57]
	v_lshlrev_b32_e32 v36, 16, v52
	v_mov_b32_e32 v37, v120
	v_add_f32_e32 v6, v9, v6
	v_add_f32_e32 v55, v114, v55
	v_pk_mul_f32 v[34:35], v[34:35], v[36:37]
	v_add_f32_e32 v6, v8, v6
	v_and_b32_e32 v8, 0xffff0000, v52
	v_mov_b32_e32 v9, v54
	v_add_f32_e32 v5, v5, v7
	v_add_f32_e32 v55, v113, v55
	v_add_f32_e32 v6, v35, v6
	v_pk_mul_f32 v[2:3], v[2:3], v[8:9]
	v_add_f32_e32 v4, v4, v5
	v_add_f32_e32 v55, v112, v55
	v_add_f32_e32 v6, v34, v6
	v_add_f32_e32 v3, v3, v4
	v_mul_f32_e32 v112, 0xbfb8aa3b, v116
	v_mul_f32_e32 v113, 0xbfb8aa3b, v55
	v_add_f32_e32 v2, v2, v3
	v_mul_f32_e32 v3, 0xbfb8aa3b, v6
	v_exp_f32_e32 v112, v112
	v_exp_f32_e32 v113, v113
	v_exp_f32_e32 v3, v3
	v_mul_f32_e32 v4, 0xbfb8aa3b, v2
	v_exp_f32_e32 v4, v4
	v_add_f32_e32 v112, 1.0, v112
	v_add_f32_e32 v113, 1.0, v113
	v_add_f32_e32 v3, 1.0, v3
	v_rcp_f32_e32 v112, v112
	v_rcp_f32_e32 v5, v113
	v_rcp_f32_e32 v3, v3
	v_add_f32_e32 v4, 1.0, v4
	v_rcp_f32_e32 v4, v4
	v_mul_f32_e32 v7, v116, v112
	v_mul_f32_e32 v9, v55, v5
	v_mul_f32_e32 v5, v6, v3
	v_mul_f32_e32 v114, v121, v117
	v_mul_f32_e32 v34, v2, v4
	v_cvt_pk_bf16_f32 v2, v29, v127
	v_cvt_pk_bf16_f32 v3, v126, v53
	v_cvt_pk_bf16_f32 v4, v124, v132
	v_cvt_pk_bf16_f32 v5, v7, v5
	v_cvt_pk_bf16_f32 v6, v128, v130
	v_cvt_pk_bf16_f32 v7, v129, v125
	v_cvt_pk_bf16_f32 v8, v131, v114
	v_cvt_pk_bf16_f32 v9, v9, v34
	ds_write_b128 v85, v[2:5] offset:8320
	ds_write_b128 v85, v[6:9] offset:8592
	s_waitcnt lgkmcnt(0)
	s_barrier
	v_cndmask_b32_e64 v3, v50, 0, s[12:13]
	v_cndmask_b32_e64 v9, v51, 0, s[12:13]
	ds_read_b32 v29, v21 offset:4604
	ds_read_b128 v[50:53], v86 offset:4096
	v_cndmask_b32_e64 v2, v49, 0, s[12:13]
	v_lshlrev_b32_e32 v4, 16, v2
	v_fma_f32 v36, v12, v4, v14
	v_lshlrev_b32_e32 v37, 16, v3
	s_waitcnt lgkmcnt(0)
	v_sub_f32_e32 v34, v29, v50
	v_mul_f32_e32 v34, 0x3fb8aa3b, v34
	v_exp_f32_e32 v113, v34
	v_lshlrev_b32_e32 v117, 16, v9
	v_lshlrev_b32_e32 v116, 16, v45
	v_mov_b32_e32 v34, v18
	v_mov_b32_e32 v35, v10
	v_fmac_f32_e32 v36, v16, v37
	v_pk_mul_f32 v[118:119], v[34:35], v[116:117]
	v_and_b32_e32 v2, 0xffff0000, v2
	v_add_f32_e32 v10, v119, v36
	v_add_f32_e32 v10, v118, v10
	v_mul_f32_e32 v18, 0xbfb8aa3b, v10
	v_exp_f32_e32 v18, v18
	v_fma_f32 v57, v13, v2, v15
	v_and_b32_e32 v49, 0xffff0000, v3
	v_lshlrev_b32_e32 v115, 16, v46
	v_add_f32_e32 v18, 1.0, v18
	v_rcp_f32_e32 v18, v18
	v_and_b32_e32 v119, 0xffff0000, v46
	v_and_b32_e32 v121, 0xffff0000, v9
	v_and_b32_e32 v120, 0xffff0000, v45
	v_mul_f32_e32 v46, v10, v18
	v_mov_b32_e32 v10, v19
	v_fmac_f32_e32 v57, v17, v49
	v_pk_mul_f32 v[18:19], v[10:11], v[120:121]
	ds_read_b128 v[2:5], v86
	ds_read_b96 v[6:8], v86 offset:16
	ds_read_b96 v[54:56], v86 offset:4112
	v_add_f32_e32 v9, v19, v57
	v_add_f32_e32 v18, v18, v9
	v_mul_f32_e32 v9, 0xbfb8aa3b, v18
	v_exp_f32_e32 v9, v9
	v_sub_f32_e32 v36, v29, v51
	v_lshlrev_b32_e32 v114, 16, v48
	v_and_b32_e32 v118, 0xffff0000, v48
	v_add_f32_e32 v9, 1.0, v9
	v_rcp_f32_e32 v112, v9
	v_mul_f32_e32 v36, 0x3fb8aa3b, v36
	v_mov_b32_e32 v123, v12
	s_waitcnt lgkmcnt(2)
	v_mov_b32_e32 v19, v2
	v_mov_b32_e32 v12, v17
	v_mov_b32_e32 v48, v121
	v_fma_f32 v2, v13, v49, v15
	v_exp_f32_e32 v51, v36
	v_mov_b32_e32 v122, v16
	v_mov_b32_e32 v36, v117
	v_pk_mul_f32 v[18:19], v[18:19], v[112:113]
	v_pk_fma_f32 v[16:17], v[12:13], v[48:49], v[2:3] op_sel_hi:[1,1,0]
	v_fma_f32 v2, v13, v121, v15
	v_pk_mul_f32 v[36:37], v[122:123], v[36:37]
	v_mul_f32_e32 v57, v46, v19
	v_mul_f32_e32 v126, v18, v19
	v_pk_fma_f32 v[18:19], v[12:13], v[120:121], v[2:3] op_sel_hi:[1,1,0]
	v_sub_f32_e32 v2, v29, v52
	v_mul_f32_e32 v2, 0x3fb8aa3b, v2
	v_lshlrev_b32_e32 v48, 16, v47
	v_and_b32_e32 v112, 0xffff0000, v47
	v_pk_mov_b32 v[46:47], v[114:115], v[116:117] op_sel:[1,0]
	v_add_f32_e32 v9, v37, v14
	v_exp_f32_e32 v45, v2
	v_sub_f32_e32 v2, v29, v53
	v_pk_mul_f32 v[52:53], v[34:35], v[46:47]
	v_add_f32_e32 v9, v36, v9
	v_add_f32_e32 v9, v53, v9
	v_pk_mul_f32 v[124:125], v[122:123], v[116:117]
	v_add_f32_e32 v9, v52, v9
	v_mul_f32_e32 v36, 0xbfb8aa3b, v9
	v_add_f32_e32 v50, v125, v14
	v_lshlrev_b32_e32 v49, 16, v44
	v_and_b32_e32 v113, 0xffff0000, v44
	v_exp_f32_e32 v44, v36
	v_pk_mul_f32 v[36:37], v[34:35], v[114:115]
	v_add_f32_e32 v50, v124, v50
	v_add_f32_e32 v37, v37, v50
	v_add_f32_e32 v36, v36, v37
	v_mul_f32_e32 v37, 0xbfb8aa3b, v36
	v_exp_f32_e32 v50, v37
	v_mul_f32_e32 v2, 0x3fb8aa3b, v2
	v_exp_f32_e32 v37, v2
	v_add_f32_e32 v2, 1.0, v44
	v_rcp_f32_e32 v44, v2
	v_add_f32_e32 v2, 1.0, v50
	v_pk_mov_b32 v[52:53], v[118:119], v[120:121] op_sel:[1,0]
	v_rcp_f32_e32 v50, v2
	v_mul_f32_e32 v2, v11, v53
	v_pk_add_f32 v[16:17], v[2:3], v[16:17] op_sel_hi:[0,1]
	v_pk_fma_f32 v[16:17], v[10:11], v[52:53], v[16:17]
	v_mul_f32_e32 v36, v36, v50
	v_mul_f32_e32 v2, 0xbfb8aa3b, v16
	v_exp_f32_e32 v2, v2
	v_mov_b32_e32 v17, v3
	v_mul_f32_e32 v9, v9, v44
	v_pk_mul_f32 v[46:47], v[122:123], v[46:47]
	v_add_f32_e32 v2, 1.0, v2
	v_rcp_f32_e32 v50, v2
	v_mul_f32_e32 v2, v11, v119
	v_pk_add_f32 v[18:19], v[2:3], v[18:19] op_sel_hi:[0,1]
	v_pk_fma_f32 v[18:19], v[10:11], v[118:119], v[18:19]
	v_pk_mul_f32 v[116:117], v[122:123], v[114:115]
	v_mul_f32_e32 v2, 0xbfb8aa3b, v18
	v_exp_f32_e32 v19, v2
	v_pk_mul_f32 v[2:3], v[16:17], v[50:51]
	v_and_b32_e32 v51, 0xffff0000, v41
	v_mul_f32_e32 v120, v9, v3
	v_add_f32_e32 v16, 1.0, v19
	v_rcp_f32_e32 v44, v16
	v_mov_b32_e32 v19, v4
	v_mul_f32_e32 v121, v2, v3
	v_fma_f32 v4, v13, v119, v15
	v_pk_mul_f32 v[2:3], v[18:19], v[44:45]
	v_pk_fma_f32 v[16:17], v[12:13], v[118:119], v[4:5] op_sel_hi:[1,1,0]
	v_mul_f32_e32 v125, v2, v3
	v_fma_f32 v2, v13, v53, v15
	s_waitcnt lgkmcnt(0)
	v_sub_f32_e32 v4, v29, v54
	v_mul_f32_e32 v124, v36, v3
	v_pk_fma_f32 v[2:3], v[12:13], v[52:53], v[2:3] op_sel_hi:[1,1,0]
	v_mul_f32_e32 v4, 0x3fb8aa3b, v4
	v_pk_mov_b32 v[52:53], v[48:49], v[114:115] op_sel:[1,0]
	v_add_f32_e32 v9, v47, v14
	v_exp_f32_e32 v19, v4
	v_sub_f32_e32 v4, v29, v55
	v_pk_mul_f32 v[54:55], v[34:35], v[52:53]
	v_add_f32_e32 v9, v46, v9
	v_add_f32_e32 v36, v117, v14
	v_add_f32_e32 v9, v55, v9
	v_pk_mul_f32 v[46:47], v[34:35], v[48:49]
	v_add_f32_e32 v36, v116, v36
	v_add_f32_e32 v9, v54, v9
	v_add_f32_e32 v36, v47, v36
	v_mul_f32_e32 v18, 0xbfb8aa3b, v9
	v_add_f32_e32 v36, v46, v36
	v_lshlrev_b32_e32 v45, 16, v41
	v_exp_f32_e32 v18, v18
	v_mul_f32_e32 v41, 0xbfb8aa3b, v36
	v_exp_f32_e32 v41, v41
	v_mul_f32_e32 v4, 0x3fb8aa3b, v4
	v_exp_f32_e32 v47, v4
	v_add_f32_e32 v4, 1.0, v18
	v_rcp_f32_e32 v18, v4
	v_add_f32_e32 v4, 1.0, v41
	v_pk_mov_b32 v[54:55], v[112:113], v[118:119] op_sel:[1,0]
	v_rcp_f32_e32 v41, v4
	v_mul_f32_e32 v4, v11, v55
	v_pk_add_f32 v[2:3], v[4:5], v[2:3] op_sel_hi:[0,1]
	v_pk_fma_f32 v[2:3], v[10:11], v[54:55], v[2:3]
	v_mul_f32_e32 v4, v11, v113
	v_mul_f32_e32 v3, 0xbfb8aa3b, v2
	v_exp_f32_e32 v3, v3
	v_pk_add_f32 v[16:17], v[4:5], v[16:17] op_sel_hi:[0,1]
	v_pk_fma_f32 v[16:17], v[10:11], v[112:113], v[16:17]
	v_mul_f32_e32 v41, v36, v41
	v_add_f32_e32 v3, 1.0, v3
	v_rcp_f32_e32 v36, v3
	v_mul_f32_e32 v3, 0xbfb8aa3b, v16
	v_exp_f32_e32 v4, v3
	v_mul_f32_e32 v9, v9, v18
	v_lshlrev_b32_e32 v44, 16, v43
	v_pk_mul_f32 v[52:53], v[122:123], v[52:53]
	v_add_f32_e32 v4, 1.0, v4
	v_rcp_f32_e32 v18, v4
	v_mov_b32_e32 v3, v5
	v_pk_mul_f32 v[2:3], v[2:3], v[36:37]
	v_mov_b32_e32 v17, v6
	v_pk_mov_b32 v[4:5], v[44:45], v[48:49] op_sel:[1,0]
	v_add_f32_e32 v6, v53, v14
	v_and_b32_e32 v50, 0xffff0000, v43
	v_mul_f32_e32 v43, v9, v3
	v_mul_f32_e32 v116, v2, v3
	v_pk_mul_f32 v[2:3], v[16:17], v[18:19]
	v_pk_mul_f32 v[16:17], v[34:35], v[4:5]
	v_add_f32_e32 v6, v52, v6
	v_add_f32_e32 v6, v17, v6
	v_add_f32_e32 v9, v16, v6
	v_mul_f32_e32 v6, 0xbfb8aa3b, v9
	v_exp_f32_e32 v6, v6
	v_pk_mul_f32 v[114:115], v[122:123], v[48:49]
	v_mul_f32_e32 v41, v41, v3
	v_mul_f32_e32 v48, v2, v3
	v_add_f32_e32 v3, 1.0, v6
	v_rcp_f32_e32 v18, v3
	v_fma_f32 v2, v13, v55, v15
	v_fma_f32 v6, v13, v113, v15
	v_pk_fma_f32 v[2:3], v[12:13], v[54:55], v[2:3] op_sel_hi:[1,1,0]
	v_mul_f32_e32 v9, v9, v18
	v_pk_mov_b32 v[18:19], v[50:51], v[112:113] op_sel:[1,0]
	v_pk_fma_f32 v[16:17], v[12:13], v[112:113], v[6:7] op_sel_hi:[1,1,0]
	v_mul_f32_e32 v6, v11, v19
	v_pk_add_f32 v[2:3], v[6:7], v[2:3] op_sel_hi:[0,1]
	v_pk_fma_f32 v[2:3], v[10:11], v[18:19], v[2:3]
	v_add_f32_e32 v6, v115, v14
	v_mul_f32_e32 v3, 0xbfb8aa3b, v2
	v_exp_f32_e32 v3, v3
	v_pk_mul_f32 v[36:37], v[34:35], v[44:45]
	v_add_f32_e32 v6, v114, v6
	v_pk_mul_f32 v[4:5], v[122:123], v[4:5]
	v_add_f32_e32 v3, 1.0, v3
	v_rcp_f32_e32 v46, v3
	v_add_f32_e32 v3, v37, v6
	v_add_f32_e32 v36, v36, v3
	v_mov_b32_e32 v3, v7
	v_mul_f32_e32 v6, v11, v51
	v_pk_mul_f32 v[2:3], v[2:3], v[46:47]
	v_pk_add_f32 v[6:7], v[6:7], v[16:17] op_sel_hi:[0,1]
	v_mul_f32_e32 v37, v9, v3
	v_pk_fma_f32 v[6:7], v[10:11], v[50:51], v[6:7]
	v_mul_f32_e32 v9, 0xbfb8aa3b, v36
	v_exp_f32_e32 v9, v9
	v_mul_f32_e32 v16, 0xbfb8aa3b, v6
	v_exp_f32_e32 v16, v16
	v_sub_f32_e32 v7, v29, v56
	v_mul_f32_e32 v7, 0x3fb8aa3b, v7
	v_exp_f32_e32 v17, v7
	v_add_f32_e32 v7, 1.0, v9
	v_rcp_f32_e32 v7, v7
	v_add_f32_e32 v9, 1.0, v16
	v_rcp_f32_e32 v16, v9
	v_mul_f32_e32 v45, v2, v3
	v_mul_f32_e32 v9, v36, v7
	v_mov_b32_e32 v7, v8
	v_pk_mul_f32 v[2:3], v[6:7], v[16:17]
	v_lshlrev_b32_e32 v8, 16, v39
	v_mul_f32_e32 v16, v9, v3
	v_mov_b32_e32 v9, v44
	v_add_f32_e32 v5, v5, v14
	v_pk_mul_f32 v[8:9], v[34:35], v[8:9]
	v_add_f32_e32 v4, v4, v5
	v_fma_f32 v6, v13, v19, v15
	v_add_f32_e32 v4, v9, v4
	v_pk_fma_f32 v[6:7], v[12:13], v[18:19], v[6:7] op_sel_hi:[1,1,0]
	v_add_f32_e32 v13, v8, v4
	ds_read2st64_b32 v[8:9], v88 offset1:16
	v_mul_f32_e32 v12, v11, v50
	v_and_b32_e32 v4, 0xffff0000, v39
	v_mov_b32_e32 v5, v50
	v_pk_add_f32 v[6:7], v[12:13], v[6:7] op_sel_hi:[0,1]
	v_pk_fma_f32 v[4:5], v[10:11], v[4:5], v[6:7]
	v_mul_f32_e32 v6, 0xbfb8aa3b, v13
	v_exp_f32_e32 v6, v6
	v_mul_f32_e32 v7, 0xbfb8aa3b, v4
	s_waitcnt lgkmcnt(0)
	v_sub_f32_e32 v5, v29, v9
	v_exp_f32_e32 v9, v7
	v_mul_f32_e32 v5, 0x3fb8aa3b, v5
	s_lshr_b32 s39, s55, 3
	v_exp_f32_e32 v7, v5
	v_add_f32_e32 v5, 1.0, v6
	s_and_b32 s39, s39, 63
	v_rcp_f32_e32 v5, v5
	v_add_f32_e32 v6, 1.0, v9
	s_lshl_b32 s58, s39, 7
	v_rcp_f32_e32 v6, v6
	s_add_i32 s58, s58, s41
	v_add_u32_e32 v18, s58, v67
	v_mul_f32_e32 v10, v13, v5
	v_mov_b32_e32 v5, v8
	s_lshl_b32 s60, s40, 6
	s_lshl_b32 s59, s40, 12
	v_mad_i64_i32 v[18:19], s[40:41], v18, s45, v[20:21]
	v_mul_f32_e32 v9, v2, v3
	v_pk_mul_f32 v[2:3], v[4:5], v[6:7]
	v_lshl_add_u64 v[34:35], v[18:19], 0, s[34:35]
	v_add_u32_e32 v18, s58, v23
	v_mul_f32_e32 v5, v10, v3
	v_mul_f32_e32 v10, v2, v3
	v_cvt_pk_bf16_f32 v2, v57, v120
	v_cvt_pk_bf16_f32 v3, v124, v43
	v_cvt_pk_bf16_f32 v4, v41, v37
	v_mad_i64_i32 v[36:37], s[40:41], v18, s45, v[20:21]
	v_add_u32_e32 v18, s58, v38
	v_mad_i64_i32 v[18:19], s[40:41], v18, s45, v[20:21]
	v_lshl_add_u64 v[38:39], v[18:19], 0, s[34:35]
	v_add_u32_e32 v18, s58, v40
	v_mad_i64_i32 v[18:19], s[40:41], v18, s45, v[20:21]
	v_lshl_add_u64 v[40:41], v[18:19], 0, s[34:35]
	v_add_u32_e32 v18, s58, v42
	s_lshl_b32 s42, s43, 3
	s_lshl_b32 s43, s39, 6
	v_mad_i64_i32 v[18:19], s[40:41], v18, s45, v[20:21]
	s_or_b32 s40, s59, s43
	s_or_b32 s40, s40, s42
	s_ashr_i32 s41, s40, 31
	v_cvt_pk_bf16_f32 v5, v16, v5
	s_lshl_b64 s[40:41], s[40:41], 2
	v_readlane_b32 s61, v253, 19
	v_cvt_pk_bf16_f32 v6, v126, v121
	v_cvt_pk_bf16_f32 v7, v125, v116
	v_cvt_pk_bf16_f32 v8, v48, v45
	v_cvt_pk_bf16_f32 v9, v9, v10
	ds_write_b128 v91, v[2:5] offset:43008
	ds_write_b128 v91, v[6:9] offset:43280
	s_add_u32 s58, s40, 0x66000000
	ds_read_b128 v[14:17], v106 offset:8192
	ds_read_b128 v[10:13], v106 offset:8256
	ds_read_b128 v[6:9], v106 offset:8320
	ds_read_b128 v[2:5], v106 offset:8384
	s_addc_u32 s61, s41, 0
	s_or_b32 s40, s60, s39
	s_ashr_i32 s41, s40, 31
	s_lshl_b64 s[40:41], s[40:41], 12
	v_lshl_add_u64 v[42:43], v[18:19], 0, s[34:35]
	v_or_b32_e32 v18, s40, v22
	v_mov_b32_e32 v19, s41
	v_or_b32_e32 v18, s38, v18
	v_readlane_b32 s62, v253, 20
	v_lshlrev_b64 v[18:19], 8, v[18:19]
	s_mov_b32 s26, 0
	v_lshl_add_u64 v[44:45], v[26:27], 0, v[18:19]
	s_mov_b64 s[38:39], 0
	s_mov_b32 s62, 0
	v_readlane_b32 s63, v253, 21
	v_readlane_b32 s64, v253, 22
	v_readlane_b32 s65, v253, 23
	v_readlane_b32 s66, v253, 24
	v_readlane_b32 s67, v253, 25
	v_readlane_b32 s68, v253, 26
	v_readlane_b32 s69, v253, 27
	v_readlane_b32 s72, v253, 30
	v_readlane_b32 s73, v253, 31
	v_readlane_b32 s74, v253, 32
	v_readlane_b32 s75, v253, 33
	s_waitcnt vmcnt(0)
	ds_write_b64 v232, v[234:235]
	ds_write_b64 v232, v[238:239] offset:256
	ds_write_b64 v233, v[236:237] offset:512
	s_mov_b32 s76, 0x45c00000
	s_mov_b32 s77, 0
	s_movk_i32 s78, 0x3000
	s_mov_b32 s79, 0
	s_movk_i32 s80, 0x6000
	s_mov_b32 s81, 0
	v_lshl_add_u64 v[190:191], s[92:93], 0, v[42:43]
	v_lshl_add_u64 v[192:193], s[92:93], 0, v[40:41]
	v_lshl_add_u64 v[194:195], s[92:93], 0, v[38:39]
	v_lshl_add_u64 v[196:197], s[92:93], 0, v[36:37]
	global_load_dword v168, v[190:191], off
	global_load_dword v169, v[192:193], off
	global_load_dword v170, v[194:195], off
	v_lshl_add_u64 v[196:197], v[196:197], 0, s[76:77]
	global_load_dword v171, v[196:197], off offset:128
	v_lshl_add_u64 v[196:197], v[196:197], 0, s[78:79]
	global_load_dword v172, v[196:197], off offset:128
	v_lshl_add_u64 v[196:197], v[196:197], 0, s[78:79]
	global_load_dword v173, v[196:197], off offset:128
	v_lshl_add_u64 v[196:197], v[196:197], 0, s[78:79]
	global_load_dword v174, v[196:197], off offset:128
	v_lshl_add_u64 v[196:197], v[196:197], 0, s[78:79]
	global_load_dword v175, v[196:197], off offset:128
	v_lshl_add_u64 v[196:197], v[196:197], 0, s[78:79]
	global_load_dword v176, v[196:197], off offset:128
	v_lshl_add_u64 v[196:197], v[196:197], 0, s[78:79]
	global_load_dword v177, v[196:197], off offset:128
	v_lshl_add_u64 v[190:191], s[92:93], 0, v[34:35]
	global_load_dword v178, v[190:191], off
	s_waitcnt lgkmcnt(0)
	s_barrier
	s_branch .LBB0_403

.Lp2_wd:
	v_cndmask_b32_e64 v18, v168, 0, s[12:13]
	v_cndmask_b32_e64 v19, v169, 0, s[12:13]
	v_cndmask_b32_e64 v20, v170, 0, s[12:13]
	v_lshlrev_b32_e32 v120, 16, v18
	v_and_b32_e32 v131, 0xffff0000, v18
	v_lshlrev_b32_e32 v121, 16, v19
	v_and_b32_e32 v132, 0xffff0000, v19
	v_lshlrev_b32_e32 v122, 16, v20
	v_and_b32_e32 v133, 0xffff0000, v20
	v_lshlrev_b32_e32 v123, 16, v171
	v_and_b32_e32 v134, 0xffff0000, v171
	v_lshlrev_b32_e32 v124, 16, v172
	v_and_b32_e32 v135, 0xffff0000, v172
	v_lshlrev_b32_e32 v125, 16, v173
	v_and_b32_e32 v136, 0xffff0000, v173
	v_lshlrev_b32_e32 v126, 16, v174
	v_and_b32_e32 v137, 0xffff0000, v174
	v_lshlrev_b32_e32 v127, 16, v175
	v_and_b32_e32 v138, 0xffff0000, v175
	v_lshlrev_b32_e32 v128, 16, v176
	v_and_b32_e32 v139, 0xffff0000, v176
	v_lshlrev_b32_e32 v129, 16, v177
	v_and_b32_e32 v140, 0xffff0000, v177
	v_lshlrev_b32_e32 v130, 16, v178
	v_and_b32_e32 v141, 0xffff0000, v178
	s_add_i32 s76, s62, 1
	s_mul_i32 s76, s76, 0x500
	v_add_u32_e32 v216, s76, v240
	ds_read_b64 v[48:49], v216
	ds_read_b64 v[56:57], v216 offset:256
	ds_read_b64 v[46:47], v216 offset:512
	ds_read_b64 v[54:55], v216 offset:768
	ds_read_b64 v[50:51], v216 offset:1024
	v_lshl_add_u64 v[34:35], v[34:35], 0, s[36:37]
	v_lshl_add_u64 v[36:37], v[36:37], 0, s[36:37]
	v_lshl_add_u64 v[38:39], v[38:39], 0, s[36:37]
	v_lshl_add_u64 v[40:41], v[40:41], 0, s[36:37]
	v_lshl_add_u64 v[42:43], v[42:43], 0, s[36:37]
	s_cmpk_eq_i32 s38, 0x600
	s_cbranch_scc1 .Lp2_pf_skip
	s_mov_b32 s76, 0x45c00000
	s_mov_b32 s77, 0
	s_movk_i32 s78, 0x3000
	s_mov_b32 s79, 0
	s_movk_i32 s80, 0x6000
	s_mov_b32 s81, 0
	v_lshl_add_u64 v[190:191], s[92:93], 0, v[42:43]
	v_lshl_add_u64 v[192:193], s[92:93], 0, v[40:41]
	v_lshl_add_u64 v[194:195], s[92:93], 0, v[38:39]
	v_lshl_add_u64 v[196:197], s[92:93], 0, v[36:37]
	global_load_dword v168, v[190:191], off
	global_load_dword v169, v[192:193], off
	global_load_dword v170, v[194:195], off
	v_lshl_add_u64 v[196:197], v[196:197], 0, s[76:77]
	global_load_dword v171, v[196:197], off offset:128
	v_lshl_add_u64 v[196:197], v[196:197], 0, s[78:79]
	global_load_dword v172, v[196:197], off offset:128
	v_lshl_add_u64 v[196:197], v[196:197], 0, s[78:79]
	global_load_dword v173, v[196:197], off offset:128
	v_lshl_add_u64 v[196:197], v[196:197], 0, s[78:79]
	global_load_dword v174, v[196:197], off offset:128
	v_lshl_add_u64 v[196:197], v[196:197], 0, s[78:79]
	global_load_dword v175, v[196:197], off offset:128
	v_lshl_add_u64 v[196:197], v[196:197], 0, s[78:79]
	global_load_dword v176, v[196:197], off offset:128
	v_lshl_add_u64 v[196:197], v[196:197], 0, s[78:79]
	global_load_dword v177, v[196:197], off offset:128
	v_lshl_add_u64 v[190:191], s[92:93], 0, v[34:35]
	global_load_dword v178, v[190:191], off
